# layer-0 norm: x row and gain kept in VGPRs, j-loop replaced by straight-line code without global loads
# baseline (speedup 1.0000x reference)
.LBB0_122:
	s_or_b64 exec, exec, s[4:5]
	s_ashr_i32 s7, s6, 31
	v_ashrrev_i32_e32 v3, 31, v2
	s_lshl_b32 s16, s23, 5
	s_waitcnt lgkmcnt(0)
	v_lshl_add_u64 v[4:5], v[2:3], 4, s[34:35]
	v_lshlrev_b32_e32 v14, 2, v2
	v_lshl_add_u32 v17, v2, 4, 0
	v_lshl_add_u64 v[2:3], v[2:3], 3, s[6:7]
	s_add_i32 s16, s16, s48
	s_mov_b64 s[10:11], 0x400
	v_lshl_add_u64 v[2:3], v[0:1], 0, v[2:3]
	s_mov_b64 s[4:5], 0x29c80200
	v_xor_b32_e32 v15, 64, v14
	v_xor_b32_e32 v16, 0x80, v14
	s_mov_b32 s17, 0
	v_lshl_add_u64 v[6:7], v[4:5], 0, s[10:11]
	v_lshl_add_u64 v[2:3], v[2:3], 0, s[4:5]
	v_mov_b32_e32 v18, 0x358637bd
	s_mov_b32 s18, 0xf800000
	v_mov_b32_e32 v19, 0x260
	s_mov_b64 s[12:13], 0x800
	s_mov_b32 s14, s16
	s_barrier
	v_add_u32_e32 v244, 0x1000, v17
	global_load_dwordx4 v[80:83], v17, s[8:9]
	global_load_dwordx4 v[84:87], v17, s[8:9] offset:1024
	global_load_dwordx4 v[88:91], v17, s[8:9] offset:2048
	global_load_dwordx4 v[92:95], v17, s[8:9] offset:3072
	global_load_dwordx4 v[96:99], v244, s[8:9]
	global_load_dwordx4 v[100:103], v244, s[8:9] offset:1024
	global_load_dwordx4 v[104:107], v244, s[8:9] offset:2048
	global_load_dwordx4 v[108:111], v244, s[8:9] offset:3072
.LBB0_123:
	s_lshl_b32 s0, s17, 3
	s_add_i32 s4, s16, s0
	s_ashr_i32 s5, s4, 31
	s_lshl_b64 s[4:5], s[4:5], 13
	v_lshl_add_u64 v[12:13], v[4:5], 0, s[4:5]
	global_load_dwordx4 v[48:51], v[12:13], off
	global_load_dwordx4 v[52:55], v[12:13], off offset:1024
	global_load_dwordx4 v[56:59], v[12:13], off offset:2048
	global_load_dwordx4 v[60:63], v[12:13], off offset:3072
	v_add_co_u32_e32 v12, vcc, s22, v12
	s_ashr_i32 s15, s14, 31
	s_nop 0
	v_addc_co_u32_e32 v13, vcc, 0, v13, vcc
	global_load_dwordx4 v[64:67], v[12:13], off
	global_load_dwordx4 v[68:71], v[12:13], off offset:1024
	global_load_dwordx4 v[72:75], v[12:13], off offset:2048
	global_load_dwordx4 v[76:79], v[12:13], off offset:3072
	s_lshl_b64 s[4:5], s[14:15], 13
	s_lshl_b64 s[20:21], s[14:15], 12
	s_waitcnt vmcnt(7)
	v_mul_f32_e32 v9, v49, v49
	v_mul_f32_e32 v11, v51, v51
	s_waitcnt vmcnt(6)
	v_mul_f32_e32 v12, v53, v53
	v_mul_f32_e32 v13, v55, v55
	s_waitcnt vmcnt(5)
	v_mul_f32_e32 v21, v57, v57
	v_mul_f32_e32 v23, v59, v59
	v_fmac_f32_e32 v9, v48, v48
	v_fmac_f32_e32 v11, v50, v50
	v_fmac_f32_e32 v12, v52, v52
	v_fmac_f32_e32 v13, v54, v54
	s_waitcnt vmcnt(4)
	v_mul_f32_e32 v25, v61, v61
	v_mul_f32_e32 v27, v63, v63
	v_fmac_f32_e32 v21, v56, v56
	v_fmac_f32_e32 v23, v58, v58
	v_add_f32_e32 v9, v9, v11
	v_add_f32_e32 v11, v12, v13
	v_fmac_f32_e32 v25, v60, v60
	v_fmac_f32_e32 v27, v62, v62
	s_waitcnt vmcnt(3)
	v_mul_f32_e32 v8, v65, v65
	v_mul_f32_e32 v10, v67, v67
	v_add_f32_e32 v12, v21, v23
	v_add_f32_e32 v9, v9, v11
	s_waitcnt vmcnt(2)
	v_mul_f32_e32 v20, v69, v69
	v_mul_f32_e32 v22, v71, v71
	v_add_f32_e32 v13, v25, v27
	v_fmac_f32_e32 v8, v64, v64
	v_fmac_f32_e32 v10, v66, v66
	v_add_f32_e32 v9, v9, v12
	s_waitcnt vmcnt(1)
	v_mul_f32_e32 v24, v73, v73
	v_mul_f32_e32 v26, v75, v75
	v_fmac_f32_e32 v20, v68, v68
	v_fmac_f32_e32 v22, v70, v70
	v_add_f32_e32 v8, v8, v10
	v_add_f32_e32 v9, v9, v13
	s_waitcnt vmcnt(0)
	v_mul_f32_e32 v28, v77, v77
	v_mul_f32_e32 v29, v79, v79
	v_fmac_f32_e32 v24, v72, v72
	v_fmac_f32_e32 v26, v74, v74
	v_add_f32_e32 v10, v20, v22
	v_add_f32_e32 v8, v9, v8
	v_fmac_f32_e32 v28, v76, v76
	v_fmac_f32_e32 v29, v78, v78
	v_add_f32_e32 v11, v24, v26
	v_add_f32_e32 v8, v8, v10
	v_add_f32_e32 v20, v28, v29
	v_add_f32_e32 v8, v8, v11
	v_add_f32_e32 v8, v8, v20
	v_mov_b32_e32 v20, v17
	s_nop 0
	v_add_f32_dpp v8, v8, v8 quad_perm:[1,0,3,2] row_mask:0xf bank_mask:0xf bound_ctrl:1
	s_nop 1
	v_add_f32_dpp v8, v8, v8 quad_perm:[2,3,0,1] row_mask:0xf bank_mask:0xf bound_ctrl:1
	s_nop 1
	v_add_f32_dpp v8, v8, v8 row_half_mirror row_mask:0xf bank_mask:0xf bound_ctrl:1
	s_nop 1
	v_add_f32_dpp v8, v8, v8 row_mirror row_mask:0xf bank_mask:0xf bound_ctrl:1
	ds_bpermute_b32 v9, v15, v8
	s_waitcnt lgkmcnt(0)
	v_add_f32_e32 v8, v8, v9
	ds_bpermute_b32 v9, v16, v8
	s_waitcnt lgkmcnt(0)
	v_add_f32_e32 v8, v8, v9
	v_fmamk_f32 v8, v8, 0x3a000000, v18
	v_mul_f32_e32 v9, 0x4f800000, v8
	v_cmp_gt_f32_e32 vcc, s18, v8
	s_nop 1
	v_cndmask_b32_e32 v10, v8, v9, vcc
	v_sqrt_f32_e32 v11, v10
	v_lshl_add_u64 v[8:9], v[6:7], 0, s[4:5]
	v_add_u32_e32 v12, -1, v11
	v_add_u32_e32 v13, 1, v11
	v_fma_f32 v21, -v12, v11, v10
	v_fma_f32 v22, -v13, v11, v10
	v_cmp_ge_f32_e64 s[4:5], 0, v21
	s_nop 1
	v_cndmask_b32_e64 v11, v11, v12, s[4:5]
	v_cmp_lt_f32_e64 s[4:5], 0, v22
	s_nop 1
	v_cndmask_b32_e64 v11, v11, v13, s[4:5]
	v_mul_f32_e32 v12, 0x37800000, v11
	v_cndmask_b32_e32 v11, v11, v12, vcc
	v_cmp_class_f32_e32 vcc, v10, v19
	s_nop 1
	v_cndmask_b32_e32 v12, v11, v10, vcc
	v_div_scale_f32 v13, s[4:5], v12, v12, 1.0
	v_rcp_f32_e32 v21, v13
	v_div_scale_f32 v22, vcc, 1.0, v12, 1.0
	v_lshl_add_u64 v[10:11], v[2:3], 0, s[20:21]
	v_fma_f32 v23, -v13, v21, 1.0
	v_fmac_f32_e32 v21, v23, v21
	v_mul_f32_e32 v23, v22, v21
	v_fma_f32 v24, -v13, v23, v22
	v_fmac_f32_e32 v23, v24, v21
	v_fma_f32 v13, -v13, v23, v22
	v_div_fmas_f32 v13, v13, v21, v23
	v_div_fixup_f32 v12, v13, v12, 1.0
	v_mov_b32_e32 v13, v12
	s_mov_b32 s4, 0
.LBB0_124:
	ds_read_b128 v[112:115], v20
	ds_read_b128 v[128:131], v20 offset:8192
	ds_read_b128 v[116:119], v20 offset:1024
	ds_read_b128 v[132:135], v20 offset:9216
	ds_read_b128 v[120:123], v20 offset:2048
	ds_read_b128 v[136:139], v20 offset:10240
	ds_read_b128 v[124:127], v20 offset:3072
	ds_read_b128 v[140:143], v20 offset:11264
	ds_read_b128 v[196:199], v20 offset:4096
	ds_read_b128 v[212:215], v20 offset:12288
	s_waitcnt lgkmcnt(8)
	v_pk_add_f32 v[128:129], v[128:129], 1.0 op_sel_hi:[1,0]
	v_pk_add_f32 v[130:131], v[130:131], 1.0 op_sel_hi:[1,0]
	v_pk_mul_f32 v[228:229], v[12:13], v[48:49]
	v_pk_mul_f32 v[230:231], v[12:13], v[50:51]
	v_pk_mul_f32 v[228:229], v[80:81], v[228:229]
	v_pk_mul_f32 v[230:231], v[82:83], v[230:231]
	v_pk_fma_f32 v[228:229], v[128:129], v[228:229], v[112:113]
	v_pk_fma_f32 v[230:231], v[130:131], v[230:231], v[114:115]
	v_cvt_pk_bf16_f32 v228, v228, v229
	v_cvt_pk_bf16_f32 v229, v230, v231
	global_store_dwordx2 v[10:11], v[228:229], off offset:-512
	ds_read_b128 v[200:203], v20 offset:5120
	ds_read_b128 v[216:219], v20 offset:13312
	s_waitcnt lgkmcnt(8)
	v_pk_add_f32 v[132:133], v[132:133], 1.0 op_sel_hi:[1,0]
	v_pk_add_f32 v[134:135], v[134:135], 1.0 op_sel_hi:[1,0]
	v_pk_mul_f32 v[232:233], v[12:13], v[52:53]
	v_pk_mul_f32 v[234:235], v[12:13], v[54:55]
	v_pk_mul_f32 v[232:233], v[84:85], v[232:233]
	v_pk_mul_f32 v[234:235], v[86:87], v[234:235]
	v_pk_fma_f32 v[232:233], v[132:133], v[232:233], v[116:117]
	v_pk_fma_f32 v[234:235], v[134:135], v[234:235], v[118:119]
	v_cvt_pk_bf16_f32 v232, v232, v233
	v_cvt_pk_bf16_f32 v233, v234, v235
	global_store_dwordx2 v[10:11], v[232:233], off
	ds_read_b128 v[204:207], v20 offset:6144
	ds_read_b128 v[220:223], v20 offset:14336
	s_waitcnt lgkmcnt(8)
	v_pk_add_f32 v[136:137], v[136:137], 1.0 op_sel_hi:[1,0]
	v_pk_add_f32 v[138:139], v[138:139], 1.0 op_sel_hi:[1,0]
	v_pk_mul_f32 v[236:237], v[12:13], v[56:57]
	v_pk_mul_f32 v[238:239], v[12:13], v[58:59]
	v_pk_mul_f32 v[236:237], v[88:89], v[236:237]
	v_pk_mul_f32 v[238:239], v[90:91], v[238:239]
	v_pk_fma_f32 v[236:237], v[136:137], v[236:237], v[120:121]
	v_pk_fma_f32 v[238:239], v[138:139], v[238:239], v[122:123]
	v_cvt_pk_bf16_f32 v236, v236, v237
	v_cvt_pk_bf16_f32 v237, v238, v239
	global_store_dwordx2 v[10:11], v[236:237], off offset:512
	ds_read_b128 v[208:211], v20 offset:7168
	ds_read_b128 v[224:227], v20 offset:15360
	s_waitcnt lgkmcnt(8)
	v_pk_add_f32 v[140:141], v[140:141], 1.0 op_sel_hi:[1,0]
	v_pk_add_f32 v[142:143], v[142:143], 1.0 op_sel_hi:[1,0]
	v_pk_mul_f32 v[240:241], v[12:13], v[60:61]
	v_pk_mul_f32 v[242:243], v[12:13], v[62:63]
	v_pk_mul_f32 v[240:241], v[92:93], v[240:241]
	v_pk_mul_f32 v[242:243], v[94:95], v[242:243]
	v_pk_fma_f32 v[240:241], v[140:141], v[240:241], v[124:125]
	v_pk_fma_f32 v[242:243], v[142:143], v[242:243], v[126:127]
	v_cvt_pk_bf16_f32 v240, v240, v241
	v_cvt_pk_bf16_f32 v241, v242, v243
	global_store_dwordx2 v[10:11], v[240:241], off offset:1024
	s_waitcnt lgkmcnt(6)
	v_pk_add_f32 v[212:213], v[212:213], 1.0 op_sel_hi:[1,0]
	v_pk_add_f32 v[214:215], v[214:215], 1.0 op_sel_hi:[1,0]
	v_pk_mul_f32 v[228:229], v[12:13], v[64:65]
	v_pk_mul_f32 v[230:231], v[12:13], v[66:67]
	v_pk_mul_f32 v[228:229], v[96:97], v[228:229]
	v_pk_mul_f32 v[230:231], v[98:99], v[230:231]
	v_pk_fma_f32 v[228:229], v[212:213], v[228:229], v[196:197]
	v_pk_fma_f32 v[230:231], v[214:215], v[230:231], v[198:199]
	v_cvt_pk_bf16_f32 v228, v228, v229
	v_cvt_pk_bf16_f32 v229, v230, v231
	global_store_dwordx2 v[10:11], v[228:229], off offset:1536
	s_waitcnt lgkmcnt(4)
	v_pk_add_f32 v[216:217], v[216:217], 1.0 op_sel_hi:[1,0]
	v_pk_add_f32 v[218:219], v[218:219], 1.0 op_sel_hi:[1,0]
	v_pk_mul_f32 v[232:233], v[12:13], v[68:69]
	v_pk_mul_f32 v[234:235], v[12:13], v[70:71]
	v_pk_mul_f32 v[232:233], v[100:101], v[232:233]
	v_pk_mul_f32 v[234:235], v[102:103], v[234:235]
	v_pk_fma_f32 v[232:233], v[216:217], v[232:233], v[200:201]
	v_pk_fma_f32 v[234:235], v[218:219], v[234:235], v[202:203]
	v_cvt_pk_bf16_f32 v232, v232, v233
	v_cvt_pk_bf16_f32 v233, v234, v235
	global_store_dwordx2 v[10:11], v[232:233], off offset:2048
	s_waitcnt lgkmcnt(2)
	v_pk_add_f32 v[220:221], v[220:221], 1.0 op_sel_hi:[1,0]
	v_pk_add_f32 v[222:223], v[222:223], 1.0 op_sel_hi:[1,0]
	v_pk_mul_f32 v[236:237], v[12:13], v[72:73]
	v_pk_mul_f32 v[238:239], v[12:13], v[74:75]
	v_pk_mul_f32 v[236:237], v[104:105], v[236:237]
	v_pk_mul_f32 v[238:239], v[106:107], v[238:239]
	v_pk_fma_f32 v[236:237], v[220:221], v[236:237], v[204:205]
	v_pk_fma_f32 v[238:239], v[222:223], v[238:239], v[206:207]
	v_cvt_pk_bf16_f32 v236, v236, v237
	v_cvt_pk_bf16_f32 v237, v238, v239
	global_store_dwordx2 v[10:11], v[236:237], off offset:2560
	s_waitcnt lgkmcnt(0)
	v_pk_add_f32 v[224:225], v[224:225], 1.0 op_sel_hi:[1,0]
	v_pk_add_f32 v[226:227], v[226:227], 1.0 op_sel_hi:[1,0]
	v_pk_mul_f32 v[240:241], v[12:13], v[76:77]
	v_pk_mul_f32 v[242:243], v[12:13], v[78:79]
	v_pk_mul_f32 v[240:241], v[108:109], v[240:241]
	v_pk_mul_f32 v[242:243], v[110:111], v[242:243]
	v_pk_fma_f32 v[240:241], v[224:225], v[240:241], v[208:209]
	v_pk_fma_f32 v[242:243], v[226:227], v[242:243], v[210:211]
	v_cvt_pk_bf16_f32 v240, v240, v241
	v_cvt_pk_bf16_f32 v241, v242, v243
	global_store_dwordx2 v[10:11], v[240:241], off offset:3072
	s_add_i32 s17, s17, 1
	s_add_i32 s14, s14, 8
	s_cmp_eq_u32 s17, 4
	s_cbranch_scc0 .LBB0_123
	s_barrier
	s_waitcnt vmcnt(0)
	v_readlane_b32 s0, v254, 5
	v_readlane_b32 s1, v254, 6
	s_barrier
	s_and_saveexec_b64 s[4:5], s[0:1]
	s_cbranch_execz .LBB0_178
	s_add_i32 s0, 0, 0x27c00
	v_mov_b32_e32 v2, s0
	s_waitcnt vmcnt(0) expcnt(0) lgkmcnt(0)
	ds_read_b32 v4, v2
	s_add_i32 s0, 0, 0x27c04
	v_mov_b32_e32 v2, s0
	ds_read_b32 v2, v2
	s_waitcnt lgkmcnt(1)
	v_cmp_ne_u32_e32 vcc, 0, v4
	s_cbranch_vccnz .LBB0_142
	s_mov_b64 s[50:51], s[34:35]
	s_load_dwordx2 s[12:13], s[58:59], 0x190
	s_load_dword s0, s[58:59], 0x198
	s_load_dwordx2 s[34:35], s[58:59], 0x188
	v_mov_b32_e32 v18, 0
	s_waitcnt lgkmcnt(0)
	s_mul_i32 s33, s13, s12
	s_mul_i32 s33, s33, s0
	s_add_u32 s8, s34, 0x1200
	s_addc_u32 s9, s35, 0
	s_add_u32 s10, s34, 0x1400
	s_addc_u32 s11, s35, 0
	s_add_u32 s12, s34, 0x1500
	s_addc_u32 s13, s35, 0
	s_add_u32 s14, s34, 0x1600
	s_addc_u32 s15, s35, 0
	s_add_u32 s16, s34, 0x1700
	s_addc_u32 s17, s35, 0
	s_add_u32 s18, s34, 0x1800
	s_addc_u32 s19, s35, 0
	s_add_u32 s20, s34, 0x1900
	s_addc_u32 s21, s35, 0
	s_add_u32 s22, s34, 0x1a00
	s_addc_u32 s23, s35, 0
	s_add_u32 s24, s34, 0x1b00
	s_addc_u32 s25, s35, 0
	s_add_u32 s26, s34, 0x1c00
	s_addc_u32 s27, s35, 0
	s_add_u32 s28, s34, 0x1d00
	s_addc_u32 s29, s35, 0
	s_add_u32 s30, s34, 0x1e00
	s_addc_u32 s31, s35, 0
	s_add_u32 s36, s34, 0x1f00
	s_addc_u32 s37, s35, 0
	s_add_u32 s38, s34, 0x2000
	s_addc_u32 s39, s35, 0
	s_add_u32 s40, s34, 0x2100
	s_addc_u32 s41, s35, 0
	s_add_u32 s42, s34, 0x2200
	s_addc_u32 s43, s35, 0
	s_add_u32 s44, s34, 0x2300
	s_addc_u32 s45, s35, 0
	s_mov_b32 s34, 1
	s_branch .LBB0_130
